# grid barrier: every workgroup writes its XCD L2 back (buffer_wbl2 sc1) before its arrival atomic; the per-XCC last arriver no longer does it after arriving (strategy 2: de-serialised release), on top
# baseline (speedup 1.0000x reference)
; __device__ __forceinline__ unsigned xb_add(unsigned* p, unsigned v) { return __hip_atomic_fetch_add(p, v, __ATOMIC_RELAXED, __HIP_MEMORY_SCOPE_AGENT); }
;     ...
;     if (lane == 0) {
;         unsigned nloc = b.st[0], nx = b.st[1], mask = b.st[2];
;         if (nloc == 0u) { xcd_barrier_complete(bar, b.x, nloc, nx, mask); b.st[0] = nloc; b.st[1] = nx; b.st[2] = mask; }
;         const unsigned old = xb_add(&bar[XB_XSUB(b.x)], 1u);
;         gen = old / nloc;
;         if (old + 1u == (gen + 1u) * nloc) {
;             __builtin_amdgcn_fence(__ATOMIC_RELEASE, "agent");
;             asm volatile("s_waitcnt vmcnt(0)" ::: "memory");
;             xb_add(&bar[XB_FLAG(b.x)], 1u);
;         }
.LBB0_236:
	s_lshl_b32 s2, s96, 8
	v_readlane_b32 s4, v254, 0
	v_readlane_b32 s5, v254, 1
	s_add_u32 s2, s4, s2
	s_addc_u32 s3, s5, 0
	s_waitcnt lgkmcnt(0)
	v_mov_b32_e32 v3, 0x1000
	v_mov_b32_e32 v4, 1
	buffer_wbl2 sc1
	s_waitcnt vmcnt(0)
	global_atomic_add v5, v3, v4, s[2:3] offset:1024 sc0
	v_cvt_f32_u32_e32 v3, v1
	v_sub_u32_e32 v6, 0, v1
	v_rcp_iflag_f32_e32 v3, v3
	s_nop 0
	v_mul_f32_e32 v3, 0x4f7ffffe, v3
	v_cvt_u32_f32_e32 v3, v3
	v_mul_lo_u32 v6, v6, v3
	v_mul_hi_u32 v6, v3, v6
	v_add_u32_e32 v3, v3, v6
	s_waitcnt vmcnt(0)
	v_mul_hi_u32 v3, v5, v3
	v_mul_lo_u32 v6, v3, v1
	v_sub_u32_e32 v6, v5, v6
	v_add_u32_e32 v7, 1, v3
	v_cmp_ge_u32_e32 vcc, v6, v1
	v_add_u32_e32 v5, 1, v5
	s_nop 0
	v_cndmask_b32_e32 v3, v3, v7, vcc
	v_sub_u32_e32 v7, v6, v1
	v_cndmask_b32_e32 v6, v6, v7, vcc
	v_add_u32_e32 v7, 1, v3
	v_cmp_ge_u32_e32 vcc, v6, v1
	s_nop 1
	v_cndmask_b32_e32 v3, v3, v7, vcc
	v_mul_lo_u32 v6, v1, v3
	v_add_u32_e32 v1, v6, v1
	v_cmp_eq_u32_e32 vcc, v5, v1
	s_and_saveexec_b64 s[4:5], vcc
	s_cbranch_execz .LBB0_238
	s_lshl_b32 s2, s96, 2
	v_readlane_b32 s6, v254, 0
	v_readlane_b32 s7, v254, 1
	s_add_u32 s2, s6, s2
	s_addc_u32 s3, s7, 0
	s_nop 0
	s_waitcnt vmcnt(0)
	v_mov_b32_e32 v1, 0x3000
	global_atomic_add v1, v4, s[2:3] offset:1536

; __device__ __forceinline__ unsigned xb_add(unsigned* p, unsigned v) { return __hip_atomic_fetch_add(p, v, __ATOMIC_RELAXED, __HIP_MEMORY_SCOPE_AGENT); }
;     ...
;     if (lane == 0) {
;         unsigned nloc = b.st[0], nx = b.st[1], mask = b.st[2];
;         if (nloc == 0u) { xcd_barrier_complete(bar, b.x, nloc, nx, mask); b.st[0] = nloc; b.st[1] = nx; b.st[2] = mask; }
;         const unsigned old = xb_add(&bar[XB_XSUB(b.x)], 1u);
;         gen = old / nloc;
;         if (old + 1u == (gen + 1u) * nloc) {
;             __builtin_amdgcn_fence(__ATOMIC_RELEASE, "agent");
;             asm volatile("s_waitcnt vmcnt(0)" ::: "memory");
;             xb_add(&bar[XB_FLAG(b.x)], 1u);
;         }
.LBB0_1448:
	s_lshl_b32 s2, s96, 8
	v_readlane_b32 s4, v254, 0
	v_readlane_b32 s5, v254, 1
	s_add_u32 s2, s4, s2
	s_addc_u32 s3, s5, 0
	s_waitcnt lgkmcnt(0)
	v_mov_b32_e32 v2, 0x1000
	v_mov_b32_e32 v3, 1
	buffer_wbl2 sc1
	s_waitcnt vmcnt(0)
	global_atomic_add v4, v2, v3, s[2:3] offset:1024 sc0
	v_cvt_f32_u32_e32 v2, v1
	v_sub_u32_e32 v5, 0, v1
	v_rcp_iflag_f32_e32 v2, v2
	s_nop 0
	v_mul_f32_e32 v2, 0x4f7ffffe, v2
	v_cvt_u32_f32_e32 v2, v2
	v_mul_lo_u32 v5, v5, v2
	v_mul_hi_u32 v5, v2, v5
	v_add_u32_e32 v2, v2, v5
	s_waitcnt vmcnt(0)
	v_mul_hi_u32 v2, v4, v2
	v_mul_lo_u32 v5, v2, v1
	v_sub_u32_e32 v5, v4, v5
	v_add_u32_e32 v6, 1, v2
	v_cmp_ge_u32_e32 vcc, v5, v1
	v_add_u32_e32 v4, 1, v4
	s_nop 0
	v_cndmask_b32_e32 v2, v2, v6, vcc
	v_sub_u32_e32 v6, v5, v1
	v_cndmask_b32_e32 v5, v5, v6, vcc
	v_add_u32_e32 v6, 1, v2
	v_cmp_ge_u32_e32 vcc, v5, v1
	s_nop 1
	v_cndmask_b32_e32 v2, v2, v6, vcc
	v_mul_lo_u32 v5, v1, v2
	v_add_u32_e32 v1, v5, v1
	v_cmp_eq_u32_e32 vcc, v4, v1
	s_and_saveexec_b64 s[4:5], vcc
	s_cbranch_execz .LBB0_1450
	s_lshl_b32 s2, s96, 2
	v_readlane_b32 s6, v254, 0
	v_readlane_b32 s7, v254, 1
	s_add_u32 s2, s6, s2
	s_addc_u32 s3, s7, 0
	s_nop 0
	s_waitcnt vmcnt(0)
	v_mov_b32_e32 v1, 0x3000
	global_atomic_add v1, v3, s[2:3] offset:1536
